# baseline (speedup 1.0000x reference)
.LBB1_8:
	s_or_b64 exec, exec, s[4:5]
	s_waitcnt vmcnt(1)
	v_mov_b32_e32 v184, 1
	v_lshl_add_u32 v180, v176, 2, v172
	v_lshl_add_u32 v181, v177, 2, v172
	v_lshl_add_u32 v182, v178, 2, v172
	v_lshl_add_u32 v183, v179, 2, v172
	ds_add_u32 v180, v184
	ds_add_u32 v181, v184
	ds_add_u32 v182, v184
	ds_add_u32 v183, v184
	s_waitcnt lgkmcnt(0)
	ds_read_b32 v151, v173
	s_waitcnt lgkmcnt(0)
	v_cvt_f32_i32_e32 v185, v151
	ds_write_b32 v173, v185 offset:256
	v_add_u32_e32 v10, v172, v2
	v_readfirstlane_b32 s4, v0
	s_waitcnt vmcnt(1) lgkmcnt(0)
	s_cmpk_lt_u32 s4, 0x100
	s_cbranch_scc0 .Lprio_done
	s_setprio 1
